# speedup vs baseline: 1.0105x; 1.0105x over previous
_Z11center_mainPKfPKcS0_Pf:
	s_load_dwordx4 s[4:7], s[0:1], 0x0
	s_load_dwordx4 s[8:11], s[0:1], 0x10
	s_and_b32 s3, s2, 7
	s_lshr_b32 s12, s2, 3
	s_mov_b32 s30, s2
	v_lshrrev_b32_e32 v1, 6, v0
	v_and_b32_e32 v2, 63, v0
	v_bfe_u32 v3, v0, 3, 3
	v_and_b32_e32 v4, 7, v0
	v_lshrrev_b32_e32 v5, 7, v0
	v_bfe_u32 v6, v0, 6, 1
	v_lshl_or_b32 v7, v5, 3, v3
	v_lshlrev_b32_e32 v8, 10, v7
	v_lshl_or_b32 v8, v6, 9, v8
	v_lshl_or_b32 v226, v4, 4, v8
	v_lshlrev_b32_e32 v17, 15, v1
	v_lshl_or_b32 v227, v2, 5, v17
	v_lshlrev_b32_e32 v237, 3, v0
	s_lshl_b32 s13, s3, 22
	s_lshl_b32 s14, s12, 15
	s_add_u32 s13, s13, s14
	s_lshl_b32 s15, s3, 18
	s_lshl_b32 s28, s3, 12
	s_waitcnt lgkmcnt(0)
	s_add_u32 s16, s4, s13
	s_addc_u32 s17, s5, 0
	global_load_dwordx4 v[194:197], v226, s[16:17] offset:0 nt
	global_load_dwordx4 v[198:201], v226, s[16:17] offset:128 nt
	global_load_dwordx4 v[202:205], v226, s[16:17] offset:256 nt
	global_load_dwordx4 v[206:209], v226, s[16:17] offset:384 nt
	s_add_u32 s8, s8, s28
	s_addc_u32 s9, s9, 0
	global_load_dwordx2 v[238:239], v237, s[8:9]
	s_add_u32 s24, s6, s15
	s_addc_u32 s25, s7, 0
	s_add_u32 s32, s24, 0x1000
	s_addc_u32 s33, s25, 0
	s_add_u32 s34, s24, 0x2000
	s_addc_u32 s35, s25, 0
	s_add_u32 s36, s24, 0x3000
	s_addc_u32 s37, s25, 0
	s_add_u32 s38, s24, 0x4000
	s_addc_u32 s39, s25, 0
	s_add_u32 s40, s24, 0x5000
	s_addc_u32 s41, s25, 0
	s_add_u32 s42, s24, 0x6000
	s_addc_u32 s43, s25, 0
	s_add_u32 s44, s24, 0x7000
	s_addc_u32 s45, s25, 0
	global_load_dwordx4 v[34:37], v227, s[24:25] offset:0
	global_load_dwordx4 v[38:41], v227, s[24:25] offset:16
	global_load_dwordx4 v[26:29], v227, s[24:25] offset:2048
	global_load_dwordx4 v[30:33], v227, s[24:25] offset:2064
	global_load_dwordx4 v[50:53], v227, s[32:33] offset:0
	global_load_dwordx4 v[54:57], v227, s[32:33] offset:16
	global_load_dwordx4 v[42:45], v227, s[32:33] offset:2048
	global_load_dwordx4 v[46:49], v227, s[32:33] offset:2064
	global_load_dwordx4 v[18:21], v227, s[34:35] offset:0
	global_load_dwordx4 v[22:25], v227, s[34:35] offset:16
	global_load_dwordx4 v[130:133], v227, s[34:35] offset:2048
	global_load_dwordx4 v[134:137], v227, s[34:35] offset:2064
	global_load_dwordx4 v[122:125], v227, s[36:37] offset:0
	global_load_dwordx4 v[126:129], v227, s[36:37] offset:16
	global_load_dwordx4 v[138:141], v227, s[36:37] offset:2048
	global_load_dwordx4 v[142:145], v227, s[36:37] offset:2064
	global_load_dwordx4 v[98:101], v227, s[38:39] offset:0
	global_load_dwordx4 v[102:105], v227, s[38:39] offset:16
	global_load_dwordx4 v[90:93], v227, s[38:39] offset:2048
	global_load_dwordx4 v[94:97], v227, s[38:39] offset:2064
	global_load_dwordx4 v[114:117], v227, s[40:41] offset:0
	global_load_dwordx4 v[118:121], v227, s[40:41] offset:16
	global_load_dwordx4 v[106:109], v227, s[40:41] offset:2048
	global_load_dwordx4 v[110:113], v227, s[40:41] offset:2064
	global_load_dwordx4 v[58:61], v227, s[42:43] offset:0
	global_load_dwordx4 v[62:65], v227, s[42:43] offset:16
	global_load_dwordx4 v[66:69], v227, s[42:43] offset:2048
	global_load_dwordx4 v[70:73], v227, s[42:43] offset:2064
	global_load_dwordx4 v[74:77], v227, s[44:45] offset:0
	global_load_dwordx4 v[78:81], v227, s[44:45] offset:16
	global_load_dwordx4 v[82:85], v227, s[44:45] offset:2048
	global_load_dwordx4 v[86:89], v227, s[44:45] offset:2064
	s_add_u32 s18, s16, 0x100000
	s_addc_u32 s19, s17, 0
	s_add_u32 s20, s16, 0x200000
	s_addc_u32 s21, s17, 0
	s_add_u32 s22, s16, 0x300000
	s_addc_u32 s23, s17, 0
	v_mul_u32_u24_e32 v9, 0x110, v7
	v_lshl_add_u32 v9, v6, 7, v9
	v_lshl_add_u32 v228, v4, 4, v9
	v_lshlrev_b32_e32 v10, 6, v7
	v_lshl_or_b32 v10, v6, 5, v10
	v_lshl_or_b32 v229, v4, 2, v10
	v_and_b32_e32 v11, 31, v0
	v_bfe_u32 v12, v0, 5, 1
	v_mul_u32_u24_e32 v13, 0x110, v11
	v_lshl_add_u32 v230, v12, 5, v13
	v_lshlrev_b32_e32 v14, 9, v1
	v_lshl_or_b32 v231, v12, 4, v14
	v_xor_b32_e32 v15, 32, v2
	v_lshlrev_b32_e32 v232, 2, v15
	v_xor_b32_e32 v15, 16, v2
	v_lshlrev_b32_e32 v247, 2, v15
	v_lshlrev_b32_e32 v16, 7, v1
	v_lshl_or_b32 v233, v11, 2, v16
	v_mov_b32_e32 v234, 0x7f7f7f7f
	s_waitcnt vmcnt(32)
	ds_write_b64 v237, v[238:239] offset:34816
	v_mul_f32_e32 v244, v194, v194
	v_mul_f32_e32 v245, v198, v198
	v_cvt_pk_fp8_f32 v240, v194, v195
	v_cvt_pk_fp8_f32 v241, v198, v199
	v_cvt_pk_fp8_f32 v242, v202, v203
	v_cvt_pk_fp8_f32 v243, v206, v207
	v_fmac_f32_e32 v244, v195, v195
	v_fmac_f32_e32 v245, v199, v199
	v_fmac_f32_e32 v244, v196, v196
	v_fmac_f32_e32 v245, v200, v200
	v_fmac_f32_e32 v244, v197, v197
	v_fmac_f32_e32 v245, v201, v201
	v_fmac_f32_e32 v244, v202, v202
	v_fmac_f32_e32 v245, v206, v206
	v_fmac_f32_e32 v244, v203, v203
	v_fmac_f32_e32 v245, v207, v207
	v_fmac_f32_e32 v244, v204, v204
	v_fmac_f32_e32 v245, v208, v208
	v_fmac_f32_e32 v244, v205, v205
	v_fmac_f32_e32 v245, v209, v209
	v_cvt_pk_fp8_f32 v240, v196, v197 op_sel:[0,0,1]
	v_cvt_pk_fp8_f32 v241, v200, v201 op_sel:[0,0,1]
	v_cvt_pk_fp8_f32 v242, v204, v205 op_sel:[0,0,1]
	v_cvt_pk_fp8_f32 v243, v208, v209 op_sel:[0,0,1]
	v_add_f32_e32 v244, v244, v245
	s_nop 0
	ds_write_b128 v228, v[240:243] offset:0
	ds_write_b32 v229, v244 offset:38912
	global_load_dwordx4 v[210:213], v226, s[18:19] offset:0 nt
	global_load_dwordx4 v[214:217], v226, s[18:19] offset:128 nt
	global_load_dwordx4 v[218:221], v226, s[18:19] offset:256 nt
	global_load_dwordx4 v[222:225], v226, s[18:19] offset:384 nt
	s_waitcnt lgkmcnt(0)
	s_barrier
	ds_read_b128 v[162:165], v230 offset:0
	ds_read_b128 v[166:169], v230 offset:16
	ds_read_b128 v[2:5], v231 offset:34816
	ds_read_b128 v[6:9], v231 offset:34848
	ds_read_b128 v[10:13], v231 offset:34880
	ds_read_b128 v[14:17], v231 offset:34912
	ds_read_b128 v[170:173], v230 offset:64
	ds_read_b128 v[174:177], v230 offset:80
	ds_read_b128 v[178:181], v230 offset:128
	ds_read_b128 v[182:185], v230 offset:144
	ds_read_b128 v[186:189], v230 offset:192
	ds_read_b128 v[190:193], v230 offset:208
	s_waitcnt vmcnt(34) lgkmcnt(6)
	v_mfma_scale_f32_32x32x64_f8f6f4 v[2:17], v[34:41], v[162:169], v[2:17], v234, v234 op_sel_hi:[0,0,0]
	s_waitcnt vmcnt(32) lgkmcnt(4)
	v_mfma_scale_f32_32x32x64_f8f6f4 v[2:17], v[26:33], v[170:177], v[2:17], v234, v234 op_sel_hi:[0,0,0]
	ds_read_b128 v[146:149], v231 offset:34944
	ds_read_b128 v[150:153], v231 offset:34976
	ds_read_b128 v[154:157], v231 offset:35008
	ds_read_b128 v[158:161], v231 offset:35040
	s_waitcnt vmcnt(30) lgkmcnt(6)
	v_mfma_scale_f32_32x32x64_f8f6f4 v[2:17], v[50:57], v[178:185], v[2:17], v234, v234 op_sel_hi:[0,0,0]
	s_waitcnt vmcnt(28) lgkmcnt(4)
	v_mfma_scale_f32_32x32x64_f8f6f4 v[2:17], v[42:49], v[186:193], v[2:17], v234, v234 op_sel_hi:[0,0,0]
	s_waitcnt lgkmcnt(0)
	s_waitcnt vmcnt(26)
	v_mfma_scale_f32_32x32x64_f8f6f4 v[146:161], v[18:25], v[162:169], v[146:161], v234, v234 op_sel_hi:[0,0,0]
	s_waitcnt vmcnt(24)
	v_mfma_scale_f32_32x32x64_f8f6f4 v[146:161], v[130:137], v[170:177], v[146:161], v234, v234 op_sel_hi:[0,0,0]
	v_min3_f32 v2, v2, v3, v4
	v_min3_f32 v5, v5, v6, v7
	v_min3_f32 v8, v8, v9, v10
	v_min3_f32 v11, v11, v12, v13
	v_min3_f32 v14, v14, v15, v16
	v_min3_f32 v2, v2, v5, v8
	v_min3_f32 v11, v11, v14, v17
	v_min_f32_e32 v235, v2, v11
	ds_read_b128 v[2:5], v231 offset:35072
	ds_read_b128 v[6:9], v231 offset:35104
	ds_read_b128 v[10:13], v231 offset:35136
	ds_read_b128 v[14:17], v231 offset:35168
	s_waitcnt vmcnt(22)
	v_mfma_scale_f32_32x32x64_f8f6f4 v[146:161], v[122:129], v[178:185], v[146:161], v234, v234 op_sel_hi:[0,0,0]
	s_waitcnt vmcnt(20)
	v_mfma_scale_f32_32x32x64_f8f6f4 v[146:161], v[138:145], v[186:193], v[146:161], v234, v234 op_sel_hi:[0,0,0]
	s_waitcnt vmcnt(18) lgkmcnt(0)
	v_mfma_scale_f32_32x32x64_f8f6f4 v[2:17], v[98:105], v[162:169], v[2:17], v234, v234 op_sel_hi:[0,0,0]
	s_waitcnt vmcnt(16)
	v_mfma_scale_f32_32x32x64_f8f6f4 v[2:17], v[90:97], v[170:177], v[2:17], v234, v234 op_sel_hi:[0,0,0]
	v_min3_f32 v146, v146, v147, v148
	v_min3_f32 v149, v149, v150, v151
	v_min3_f32 v152, v152, v153, v154
	v_min3_f32 v155, v155, v156, v157
	v_min3_f32 v158, v158, v159, v160
	v_min3_f32 v146, v146, v149, v152
	v_min3_f32 v155, v155, v158, v161
	v_min3_f32 v235, v235, v146, v155
	ds_read_b128 v[146:149], v231 offset:35200
	ds_read_b128 v[150:153], v231 offset:35232
	ds_read_b128 v[154:157], v231 offset:35264
	ds_read_b128 v[158:161], v231 offset:35296
	s_waitcnt vmcnt(14)
	v_mfma_scale_f32_32x32x64_f8f6f4 v[2:17], v[114:121], v[178:185], v[2:17], v234, v234 op_sel_hi:[0,0,0]
	s_waitcnt vmcnt(12)
	v_mfma_scale_f32_32x32x64_f8f6f4 v[2:17], v[106:113], v[186:193], v[2:17], v234, v234 op_sel_hi:[0,0,0]
	s_waitcnt vmcnt(10) lgkmcnt(0)
	v_mfma_scale_f32_32x32x64_f8f6f4 v[146:161], v[58:65], v[162:169], v[146:161], v234, v234 op_sel_hi:[0,0,0]
	s_waitcnt vmcnt(8)
	v_mfma_scale_f32_32x32x64_f8f6f4 v[146:161], v[66:73], v[170:177], v[146:161], v234, v234 op_sel_hi:[0,0,0]
	v_min3_f32 v2, v2, v3, v4
	v_min3_f32 v5, v5, v6, v7
	v_min3_f32 v8, v8, v9, v10
	v_min3_f32 v11, v11, v12, v13
	v_min3_f32 v14, v14, v15, v16
	v_min3_f32 v2, v2, v5, v8
	v_min3_f32 v11, v11, v14, v17
	v_min3_f32 v235, v235, v2, v11
	ds_read_b128 v[2:5], v231 offset:34816
	ds_read_b128 v[6:9], v231 offset:34848
	ds_read_b128 v[10:13], v231 offset:34880
	ds_read_b128 v[14:17], v231 offset:34912
	s_waitcnt vmcnt(6)
	v_mfma_scale_f32_32x32x64_f8f6f4 v[146:161], v[74:81], v[178:185], v[146:161], v234, v234 op_sel_hi:[0,0,0]
	s_waitcnt vmcnt(4)
	v_mfma_scale_f32_32x32x64_f8f6f4 v[146:161], v[82:89], v[186:193], v[146:161], v234, v234 op_sel_hi:[0,0,0]
	s_waitcnt vmcnt(0)
	v_mul_f32_e32 v244, v210, v210
	v_mul_f32_e32 v245, v214, v214
	v_cvt_pk_fp8_f32 v240, v210, v211
	v_cvt_pk_fp8_f32 v241, v214, v215
	v_cvt_pk_fp8_f32 v242, v218, v219
	v_cvt_pk_fp8_f32 v243, v222, v223
	v_fmac_f32_e32 v244, v211, v211
	v_fmac_f32_e32 v245, v215, v215
	v_fmac_f32_e32 v244, v212, v212
	v_fmac_f32_e32 v245, v216, v216
	v_fmac_f32_e32 v244, v213, v213
	v_fmac_f32_e32 v245, v217, v217
	v_fmac_f32_e32 v244, v218, v218
	v_fmac_f32_e32 v245, v222, v222
	v_fmac_f32_e32 v244, v219, v219
	v_fmac_f32_e32 v245, v223, v223
	v_fmac_f32_e32 v244, v220, v220
	v_fmac_f32_e32 v245, v224, v224
	v_fmac_f32_e32 v244, v221, v221
	v_fmac_f32_e32 v245, v225, v225
	v_cvt_pk_fp8_f32 v240, v212, v213 op_sel:[0,0,1]
	v_cvt_pk_fp8_f32 v241, v216, v217 op_sel:[0,0,1]
	v_cvt_pk_fp8_f32 v242, v220, v221 op_sel:[0,0,1]
	v_cvt_pk_fp8_f32 v243, v224, v225 op_sel:[0,0,1]
	v_add_f32_e32 v244, v244, v245
	s_nop 0
	ds_write_b128 v228, v[240:243] offset:8704
	ds_write_b32 v229, v244 offset:40960
	global_load_dwordx4 v[194:197], v226, s[20:21] offset:0 nt
	global_load_dwordx4 v[198:201], v226, s[20:21] offset:128 nt
	global_load_dwordx4 v[202:205], v226, s[20:21] offset:256 nt
	global_load_dwordx4 v[206:209], v226, s[20:21] offset:384 nt
	s_waitcnt lgkmcnt(0)
	s_barrier
	ds_read_b128 v[162:165], v230 offset:8704
	ds_read_b128 v[166:169], v230 offset:8720
	ds_read_b128 v[170:173], v230 offset:8768
	ds_read_b128 v[174:177], v230 offset:8784
	ds_read_b128 v[178:181], v230 offset:8832
	ds_read_b128 v[182:185], v230 offset:8848
	ds_read_b128 v[186:189], v230 offset:8896
	ds_read_b128 v[190:193], v230 offset:8912
	s_waitcnt lgkmcnt(6)
	v_mfma_scale_f32_32x32x64_f8f6f4 v[2:17], v[34:41], v[162:169], v[2:17], v234, v234 op_sel_hi:[0,0,0]
	s_waitcnt lgkmcnt(4)
	v_mfma_scale_f32_32x32x64_f8f6f4 v[2:17], v[26:33], v[170:177], v[2:17], v234, v234 op_sel_hi:[0,0,0]
	v_min3_f32 v146, v146, v147, v148
	v_min3_f32 v149, v149, v150, v151
	v_min3_f32 v152, v152, v153, v154
	v_min3_f32 v155, v155, v156, v157
	v_min3_f32 v158, v158, v159, v160
	v_min3_f32 v146, v146, v149, v152
	v_min3_f32 v155, v155, v158, v161
	v_min3_f32 v235, v235, v146, v155
	ds_bpermute_b32 v246, v232, v235
	ds_read_b128 v[146:149], v231 offset:34944
	ds_read_b128 v[150:153], v231 offset:34976
	ds_read_b128 v[154:157], v231 offset:35008
	ds_read_b128 v[158:161], v231 offset:35040
	s_waitcnt lgkmcnt(7)
	v_mfma_scale_f32_32x32x64_f8f6f4 v[2:17], v[50:57], v[178:185], v[2:17], v234, v234 op_sel_hi:[0,0,0]
	s_waitcnt lgkmcnt(5)
	v_mfma_scale_f32_32x32x64_f8f6f4 v[2:17], v[42:49], v[186:193], v[2:17], v234, v234 op_sel_hi:[0,0,0]
	s_waitcnt lgkmcnt(0)
	v_min_f32_e32 v246, v235, v246
	ds_write_b32 v233, v246 offset:47104
	v_mfma_scale_f32_32x32x64_f8f6f4 v[146:161], v[18:25], v[162:169], v[146:161], v234, v234 op_sel_hi:[0,0,0]
	v_mfma_scale_f32_32x32x64_f8f6f4 v[146:161], v[130:137], v[170:177], v[146:161], v234, v234 op_sel_hi:[0,0,0]
	v_min3_f32 v2, v2, v3, v4
	v_min3_f32 v5, v5, v6, v7
	v_min3_f32 v8, v8, v9, v10
	v_min3_f32 v11, v11, v12, v13
	v_min3_f32 v14, v14, v15, v16
	v_min3_f32 v2, v2, v5, v8
	v_min3_f32 v11, v11, v14, v17
	v_min_f32_e32 v236, v2, v11
	ds_read_b128 v[2:5], v231 offset:35072
	ds_read_b128 v[6:9], v231 offset:35104
	ds_read_b128 v[10:13], v231 offset:35136
	ds_read_b128 v[14:17], v231 offset:35168
	v_mfma_scale_f32_32x32x64_f8f6f4 v[146:161], v[122:129], v[178:185], v[146:161], v234, v234 op_sel_hi:[0,0,0]
	v_mfma_scale_f32_32x32x64_f8f6f4 v[146:161], v[138:145], v[186:193], v[146:161], v234, v234 op_sel_hi:[0,0,0]
	s_waitcnt lgkmcnt(0)
	v_mfma_scale_f32_32x32x64_f8f6f4 v[2:17], v[98:105], v[162:169], v[2:17], v234, v234 op_sel_hi:[0,0,0]
	v_mfma_scale_f32_32x32x64_f8f6f4 v[2:17], v[90:97], v[170:177], v[2:17], v234, v234 op_sel_hi:[0,0,0]
	v_min3_f32 v146, v146, v147, v148
	v_min3_f32 v149, v149, v150, v151
	v_min3_f32 v152, v152, v153, v154
	v_min3_f32 v155, v155, v156, v157
	v_min3_f32 v158, v158, v159, v160
	v_min3_f32 v146, v146, v149, v152
	v_min3_f32 v155, v155, v158, v161
	v_min3_f32 v236, v236, v146, v155
	ds_read_b128 v[146:149], v231 offset:35200
	ds_read_b128 v[150:153], v231 offset:35232
	ds_read_b128 v[154:157], v231 offset:35264
	ds_read_b128 v[158:161], v231 offset:35296
	v_mfma_scale_f32_32x32x64_f8f6f4 v[2:17], v[114:121], v[178:185], v[2:17], v234, v234 op_sel_hi:[0,0,0]
	v_mfma_scale_f32_32x32x64_f8f6f4 v[2:17], v[106:113], v[186:193], v[2:17], v234, v234 op_sel_hi:[0,0,0]
	s_waitcnt lgkmcnt(0)
	v_mfma_scale_f32_32x32x64_f8f6f4 v[146:161], v[58:65], v[162:169], v[146:161], v234, v234 op_sel_hi:[0,0,0]
	v_mfma_scale_f32_32x32x64_f8f6f4 v[146:161], v[66:73], v[170:177], v[146:161], v234, v234 op_sel_hi:[0,0,0]
	v_min3_f32 v2, v2, v3, v4
	v_min3_f32 v5, v5, v6, v7
	v_min3_f32 v8, v8, v9, v10
	v_min3_f32 v11, v11, v12, v13
	v_min3_f32 v14, v14, v15, v16
	v_min3_f32 v2, v2, v5, v8
	v_min3_f32 v11, v11, v14, v17
	v_min3_f32 v236, v236, v2, v11
	ds_read_b128 v[2:5], v231 offset:34816
	ds_read_b128 v[6:9], v231 offset:34848
	ds_read_b128 v[10:13], v231 offset:34880
	ds_read_b128 v[14:17], v231 offset:34912
	v_mfma_scale_f32_32x32x64_f8f6f4 v[146:161], v[74:81], v[178:185], v[146:161], v234, v234 op_sel_hi:[0,0,0]
	v_mfma_scale_f32_32x32x64_f8f6f4 v[146:161], v[82:89], v[186:193], v[146:161], v234, v234 op_sel_hi:[0,0,0]
	s_waitcnt vmcnt(0)
	v_mul_f32_e32 v244, v194, v194
	v_mul_f32_e32 v245, v198, v198
	v_cvt_pk_fp8_f32 v240, v194, v195
	v_cvt_pk_fp8_f32 v241, v198, v199
	v_cvt_pk_fp8_f32 v242, v202, v203
	v_cvt_pk_fp8_f32 v243, v206, v207
	v_fmac_f32_e32 v244, v195, v195
	v_fmac_f32_e32 v245, v199, v199
	v_fmac_f32_e32 v244, v196, v196
	v_fmac_f32_e32 v245, v200, v200
	v_fmac_f32_e32 v244, v197, v197
	v_fmac_f32_e32 v245, v201, v201
	v_fmac_f32_e32 v244, v202, v202
	v_fmac_f32_e32 v245, v206, v206
	v_fmac_f32_e32 v244, v203, v203
	v_fmac_f32_e32 v245, v207, v207
	v_fmac_f32_e32 v244, v204, v204
	v_fmac_f32_e32 v245, v208, v208
	v_fmac_f32_e32 v244, v205, v205
	v_fmac_f32_e32 v245, v209, v209
	v_cvt_pk_fp8_f32 v240, v196, v197 op_sel:[0,0,1]
	v_cvt_pk_fp8_f32 v241, v200, v201 op_sel:[0,0,1]
	v_cvt_pk_fp8_f32 v242, v204, v205 op_sel:[0,0,1]
	v_cvt_pk_fp8_f32 v243, v208, v209 op_sel:[0,0,1]
	v_add_f32_e32 v244, v244, v245
	s_nop 0
	ds_write_b128 v228, v[240:243] offset:17408
	ds_write_b32 v229, v244 offset:43008
	global_load_dwordx4 v[210:213], v226, s[22:23] offset:0 nt
	global_load_dwordx4 v[214:217], v226, s[22:23] offset:128 nt
	global_load_dwordx4 v[218:221], v226, s[22:23] offset:256 nt
	global_load_dwordx4 v[222:225], v226, s[22:23] offset:384 nt
	s_waitcnt lgkmcnt(0)
	s_barrier
	ds_read_b128 v[162:165], v230 offset:17408
	ds_read_b128 v[166:169], v230 offset:17424
	ds_read_b128 v[170:173], v230 offset:17472
	ds_read_b128 v[174:177], v230 offset:17488
	ds_read_b128 v[178:181], v230 offset:17536
	ds_read_b128 v[182:185], v230 offset:17552
	ds_read_b128 v[186:189], v230 offset:17600
	ds_read_b128 v[190:193], v230 offset:17616
	s_waitcnt lgkmcnt(6)
	v_mfma_scale_f32_32x32x64_f8f6f4 v[2:17], v[34:41], v[162:169], v[2:17], v234, v234 op_sel_hi:[0,0,0]
	s_waitcnt lgkmcnt(4)
	v_mfma_scale_f32_32x32x64_f8f6f4 v[2:17], v[26:33], v[170:177], v[2:17], v234, v234 op_sel_hi:[0,0,0]
	v_min3_f32 v146, v146, v147, v148
	v_min3_f32 v149, v149, v150, v151
	v_min3_f32 v152, v152, v153, v154
	v_min3_f32 v155, v155, v156, v157
	v_min3_f32 v158, v158, v159, v160
	v_min3_f32 v146, v146, v149, v152
	v_min3_f32 v155, v155, v158, v161
	v_min3_f32 v236, v236, v146, v155
	ds_bpermute_b32 v246, v232, v236
	ds_read_b128 v[146:149], v231 offset:34944
	ds_read_b128 v[150:153], v231 offset:34976
	ds_read_b128 v[154:157], v231 offset:35008
	ds_read_b128 v[158:161], v231 offset:35040
	s_waitcnt lgkmcnt(7)
	v_mfma_scale_f32_32x32x64_f8f6f4 v[2:17], v[50:57], v[178:185], v[2:17], v234, v234 op_sel_hi:[0,0,0]
	s_waitcnt lgkmcnt(5)
	v_mfma_scale_f32_32x32x64_f8f6f4 v[2:17], v[42:49], v[186:193], v[2:17], v234, v234 op_sel_hi:[0,0,0]
	s_waitcnt lgkmcnt(0)
	v_min_f32_e32 v246, v236, v246
	ds_write_b32 v233, v246 offset:48128
	v_mfma_scale_f32_32x32x64_f8f6f4 v[146:161], v[18:25], v[162:169], v[146:161], v234, v234 op_sel_hi:[0,0,0]
	v_mfma_scale_f32_32x32x64_f8f6f4 v[146:161], v[130:137], v[170:177], v[146:161], v234, v234 op_sel_hi:[0,0,0]
	v_min3_f32 v2, v2, v3, v4
	v_min3_f32 v5, v5, v6, v7
	v_min3_f32 v8, v8, v9, v10
	v_min3_f32 v11, v11, v12, v13
	v_min3_f32 v14, v14, v15, v16
	v_min3_f32 v2, v2, v5, v8
	v_min3_f32 v11, v11, v14, v17
	v_min_f32_e32 v235, v2, v11
	ds_read_b128 v[2:5], v231 offset:35072
	ds_read_b128 v[6:9], v231 offset:35104
	ds_read_b128 v[10:13], v231 offset:35136
	ds_read_b128 v[14:17], v231 offset:35168
	v_mfma_scale_f32_32x32x64_f8f6f4 v[146:161], v[122:129], v[178:185], v[146:161], v234, v234 op_sel_hi:[0,0,0]
	v_mfma_scale_f32_32x32x64_f8f6f4 v[146:161], v[138:145], v[186:193], v[146:161], v234, v234 op_sel_hi:[0,0,0]
	s_waitcnt lgkmcnt(0)
	v_mfma_scale_f32_32x32x64_f8f6f4 v[2:17], v[98:105], v[162:169], v[2:17], v234, v234 op_sel_hi:[0,0,0]
	v_mfma_scale_f32_32x32x64_f8f6f4 v[2:17], v[90:97], v[170:177], v[2:17], v234, v234 op_sel_hi:[0,0,0]
	v_min3_f32 v146, v146, v147, v148
	v_min3_f32 v149, v149, v150, v151
	v_min3_f32 v152, v152, v153, v154
	v_min3_f32 v155, v155, v156, v157
	v_min3_f32 v158, v158, v159, v160
	v_min3_f32 v146, v146, v149, v152
	v_min3_f32 v155, v155, v158, v161
	v_min3_f32 v235, v235, v146, v155
	ds_read_b128 v[146:149], v231 offset:35200
	ds_read_b128 v[150:153], v231 offset:35232
	ds_read_b128 v[154:157], v231 offset:35264
	ds_read_b128 v[158:161], v231 offset:35296
	v_mfma_scale_f32_32x32x64_f8f6f4 v[2:17], v[114:121], v[178:185], v[2:17], v234, v234 op_sel_hi:[0,0,0]
	v_mfma_scale_f32_32x32x64_f8f6f4 v[2:17], v[106:113], v[186:193], v[2:17], v234, v234 op_sel_hi:[0,0,0]
	s_waitcnt lgkmcnt(0)
	v_mfma_scale_f32_32x32x64_f8f6f4 v[146:161], v[58:65], v[162:169], v[146:161], v234, v234 op_sel_hi:[0,0,0]
	v_mfma_scale_f32_32x32x64_f8f6f4 v[146:161], v[66:73], v[170:177], v[146:161], v234, v234 op_sel_hi:[0,0,0]
	v_min3_f32 v2, v2, v3, v4
	v_min3_f32 v5, v5, v6, v7
	v_min3_f32 v8, v8, v9, v10
	v_min3_f32 v11, v11, v12, v13
	v_min3_f32 v14, v14, v15, v16
	v_min3_f32 v2, v2, v5, v8
	v_min3_f32 v11, v11, v14, v17
	v_min3_f32 v235, v235, v2, v11
	ds_read_b128 v[2:5], v231 offset:34816
	ds_read_b128 v[6:9], v231 offset:34848
	ds_read_b128 v[10:13], v231 offset:34880
	ds_read_b128 v[14:17], v231 offset:34912
	v_mfma_scale_f32_32x32x64_f8f6f4 v[146:161], v[74:81], v[178:185], v[146:161], v234, v234 op_sel_hi:[0,0,0]
	v_mfma_scale_f32_32x32x64_f8f6f4 v[146:161], v[82:89], v[186:193], v[146:161], v234, v234 op_sel_hi:[0,0,0]
	s_waitcnt vmcnt(0)
	v_mul_f32_e32 v244, v210, v210
	v_mul_f32_e32 v245, v214, v214
	v_cvt_pk_fp8_f32 v240, v210, v211
	v_cvt_pk_fp8_f32 v241, v214, v215
	v_cvt_pk_fp8_f32 v242, v218, v219
	v_cvt_pk_fp8_f32 v243, v222, v223
	v_fmac_f32_e32 v244, v211, v211
	v_fmac_f32_e32 v245, v215, v215
	v_fmac_f32_e32 v244, v212, v212
	v_fmac_f32_e32 v245, v216, v216
	v_fmac_f32_e32 v244, v213, v213
	v_fmac_f32_e32 v245, v217, v217
	v_fmac_f32_e32 v244, v218, v218
	v_fmac_f32_e32 v245, v222, v222
	v_fmac_f32_e32 v244, v219, v219
	v_fmac_f32_e32 v245, v223, v223
	v_fmac_f32_e32 v244, v220, v220
	v_fmac_f32_e32 v245, v224, v224
	v_fmac_f32_e32 v244, v221, v221
	v_fmac_f32_e32 v245, v225, v225
	v_cvt_pk_fp8_f32 v240, v212, v213 op_sel:[0,0,1]
	v_cvt_pk_fp8_f32 v241, v216, v217 op_sel:[0,0,1]
	v_cvt_pk_fp8_f32 v242, v220, v221 op_sel:[0,0,1]
	v_cvt_pk_fp8_f32 v243, v224, v225 op_sel:[0,0,1]
	v_add_f32_e32 v244, v244, v245
	s_nop 0
	ds_write_b128 v228, v[240:243] offset:26112
	ds_write_b32 v229, v244 offset:45056
	s_waitcnt lgkmcnt(0)
	s_barrier
	ds_read_b128 v[162:165], v230 offset:26112
	ds_read_b128 v[166:169], v230 offset:26128
	ds_read_b128 v[170:173], v230 offset:26176
	ds_read_b128 v[174:177], v230 offset:26192
	ds_read_b128 v[178:181], v230 offset:26240
	ds_read_b128 v[182:185], v230 offset:26256
	ds_read_b128 v[186:189], v230 offset:26304
	ds_read_b128 v[190:193], v230 offset:26320
	s_waitcnt lgkmcnt(6)
	v_mfma_scale_f32_32x32x64_f8f6f4 v[2:17], v[34:41], v[162:169], v[2:17], v234, v234 op_sel_hi:[0,0,0]
	s_waitcnt lgkmcnt(4)
	v_mfma_scale_f32_32x32x64_f8f6f4 v[2:17], v[26:33], v[170:177], v[2:17], v234, v234 op_sel_hi:[0,0,0]
	v_min3_f32 v146, v146, v147, v148
	v_min3_f32 v149, v149, v150, v151
	v_min3_f32 v152, v152, v153, v154
	v_min3_f32 v155, v155, v156, v157
	v_min3_f32 v158, v158, v159, v160
	v_min3_f32 v146, v146, v149, v152
	v_min3_f32 v155, v155, v158, v161
	v_min3_f32 v235, v235, v146, v155
	ds_bpermute_b32 v246, v232, v235
	ds_read_b128 v[146:149], v231 offset:34944
	ds_read_b128 v[150:153], v231 offset:34976
	ds_read_b128 v[154:157], v231 offset:35008
	ds_read_b128 v[158:161], v231 offset:35040
	s_waitcnt lgkmcnt(7)
	v_mfma_scale_f32_32x32x64_f8f6f4 v[2:17], v[50:57], v[178:185], v[2:17], v234, v234 op_sel_hi:[0,0,0]
	s_waitcnt lgkmcnt(5)
	v_mfma_scale_f32_32x32x64_f8f6f4 v[2:17], v[42:49], v[186:193], v[2:17], v234, v234 op_sel_hi:[0,0,0]
	s_waitcnt lgkmcnt(0)
	v_min_f32_e32 v246, v235, v246
	ds_write_b32 v233, v246 offset:49152
	v_mfma_scale_f32_32x32x64_f8f6f4 v[146:161], v[18:25], v[162:169], v[146:161], v234, v234 op_sel_hi:[0,0,0]
	v_mfma_scale_f32_32x32x64_f8f6f4 v[146:161], v[130:137], v[170:177], v[146:161], v234, v234 op_sel_hi:[0,0,0]
	v_min3_f32 v2, v2, v3, v4
	v_min3_f32 v5, v5, v6, v7
	v_min3_f32 v8, v8, v9, v10
	v_min3_f32 v11, v11, v12, v13
	v_min3_f32 v14, v14, v15, v16
	v_min3_f32 v2, v2, v5, v8
	v_min3_f32 v11, v11, v14, v17
	v_min_f32_e32 v236, v2, v11
	ds_read_b128 v[2:5], v231 offset:35072
	ds_read_b128 v[6:9], v231 offset:35104
	ds_read_b128 v[10:13], v231 offset:35136
	ds_read_b128 v[14:17], v231 offset:35168
	v_mfma_scale_f32_32x32x64_f8f6f4 v[146:161], v[122:129], v[178:185], v[146:161], v234, v234 op_sel_hi:[0,0,0]
	v_mfma_scale_f32_32x32x64_f8f6f4 v[146:161], v[138:145], v[186:193], v[146:161], v234, v234 op_sel_hi:[0,0,0]
	s_waitcnt lgkmcnt(0)
	v_mfma_scale_f32_32x32x64_f8f6f4 v[2:17], v[98:105], v[162:169], v[2:17], v234, v234 op_sel_hi:[0,0,0]
	v_mfma_scale_f32_32x32x64_f8f6f4 v[2:17], v[90:97], v[170:177], v[2:17], v234, v234 op_sel_hi:[0,0,0]
	v_min3_f32 v146, v146, v147, v148
	v_min3_f32 v149, v149, v150, v151
	v_min3_f32 v152, v152, v153, v154
	v_min3_f32 v155, v155, v156, v157
	v_min3_f32 v158, v158, v159, v160
	v_min3_f32 v146, v146, v149, v152
	v_min3_f32 v155, v155, v158, v161
	v_min3_f32 v236, v236, v146, v155
	ds_read_b128 v[146:149], v231 offset:35200
	ds_read_b128 v[150:153], v231 offset:35232
	ds_read_b128 v[154:157], v231 offset:35264
	ds_read_b128 v[158:161], v231 offset:35296
	v_mfma_scale_f32_32x32x64_f8f6f4 v[2:17], v[114:121], v[178:185], v[2:17], v234, v234 op_sel_hi:[0,0,0]
	v_mfma_scale_f32_32x32x64_f8f6f4 v[2:17], v[106:113], v[186:193], v[2:17], v234, v234 op_sel_hi:[0,0,0]
	s_waitcnt lgkmcnt(0)
	v_mfma_scale_f32_32x32x64_f8f6f4 v[146:161], v[58:65], v[162:169], v[146:161], v234, v234 op_sel_hi:[0,0,0]
	v_mfma_scale_f32_32x32x64_f8f6f4 v[146:161], v[66:73], v[170:177], v[146:161], v234, v234 op_sel_hi:[0,0,0]
	v_min3_f32 v2, v2, v3, v4
	v_min3_f32 v5, v5, v6, v7
	v_min3_f32 v8, v8, v9, v10
	v_min3_f32 v11, v11, v12, v13
	v_min3_f32 v14, v14, v15, v16
	v_min3_f32 v2, v2, v5, v8
	v_min3_f32 v11, v11, v14, v17
	v_min3_f32 v236, v236, v2, v11
	v_mfma_scale_f32_32x32x64_f8f6f4 v[146:161], v[74:81], v[178:185], v[146:161], v234, v234 op_sel_hi:[0,0,0]
	v_mfma_scale_f32_32x32x64_f8f6f4 v[146:161], v[82:89], v[186:193], v[146:161], v234, v234 op_sel_hi:[0,0,0]
	v_cmp_gt_u32_e32 vcc, 0x80, v0
	s_and_saveexec_b64 s[34:35], vcc
	v_lshlrev_b32_e32 v36, 6, v0
	ds_read_b128 v[20:23], v36 offset:38912
	ds_read_b128 v[24:27], v36 offset:38928
	ds_read_b128 v[28:31], v36 offset:38944
	ds_read_b128 v[32:35], v36 offset:38960
	s_mov_b64 exec, s[34:35]
	s_nop 15
	s_nop 3
	v_min3_f32 v146, v146, v147, v148
	v_min3_f32 v149, v149, v150, v151
	v_min3_f32 v152, v152, v153, v154
	v_min3_f32 v155, v155, v156, v157
	v_min3_f32 v158, v158, v159, v160
	v_min3_f32 v146, v146, v149, v152
	v_min3_f32 v155, v155, v158, v161
	v_min3_f32 v236, v236, v146, v155
	ds_bpermute_b32 v246, v232, v236
	s_waitcnt lgkmcnt(0)
	v_min_f32_e32 v246, v236, v246
	ds_write_b32 v233, v246 offset:50176
	s_waitcnt lgkmcnt(0)
	s_barrier
	v_readfirstlane_b32 s2, v1
	s_nop 3
	s_cmp_gt_u32 s2, 1
	s_cbranch_scc1 .Lmain_end
	v_and_b32_e32 v2, 31, v0
	v_lshlrev_b32_e32 v3, 5, v0
	v_and_b32_e32 v3, 0xc00, v3
	v_lshl_or_b32 v8, v2, 2, v3
	v_add_u32_e32 v8, 0xb800, v8
	ds_read2_b32 v[2:3], v8 offset1:32
	ds_read2_b32 v[4:5], v8 offset0:64 offset1:96
	ds_read2_b32 v[6:7], v8 offset0:128 offset1:160
	ds_read2_b32 v[10:11], v8 offset0:192 offset1:224
	s_mov_b32 s8, 0xf800000
	s_lshr_b32 s2, s30, 3
	s_lshl_b32 s2, s2, 7
	s_add_u32 s2, s2, 0x300000
	s_add_u32 s6, s6, s2
	s_addc_u32 s7, s7, 0
	s_mov_b32 s4, 0
	s_mov_b32 s5, 0x41d00000
	s_mov_b32 s16, 0
	s_mov_b32 s17, 0x420e0000
	s_waitcnt lgkmcnt(0)
	v_min3_f32 v2, v2, v3, v4
	v_min3_f32 v5, v5, v6, v7
	v_min3_f32 v2, v2, v10, v11
	v_min_f32_e32 v2, v2, v5
	s_waitcnt lgkmcnt(0)
	v_add_f32_e32 v20, v20, v21
	v_add_f32_e32 v22, v22, v23
	v_add_f32_e32 v24, v24, v25
	v_add_f32_e32 v26, v26, v27
	v_add_f32_e32 v28, v28, v29
	v_add_f32_e32 v30, v30, v31
	v_add_f32_e32 v32, v32, v33
	v_add_f32_e32 v34, v34, v35
	v_add_f32_e32 v20, v20, v22
	v_add_f32_e32 v24, v24, v26
	v_add_f32_e32 v28, v28, v30
	v_add_f32_e32 v32, v32, v34
	v_add_f32_e32 v20, v20, v24
	v_add_f32_e32 v28, v28, v32
	v_add_f32_e32 v20, v20, v28
	v_add_f32_e32 v2, v2, v20
	v_max_f32_e32 v2, 0, v2
	v_mul_f32_e32 v3, 0x4f800000, v2
	v_cmp_gt_f32_e32 vcc, s8, v2
	s_nop 1
	v_cndmask_b32_e32 v2, v2, v3, vcc
	v_sqrt_f32_e32 v3, v2
	s_nop 0
	v_add_u32_e32 v4, -1, v3
	v_fma_f32 v5, -v4, v3, v2
	v_cmp_ge_f32_e64 s[18:19], 0, v5
	v_add_u32_e32 v5, 1, v3
	s_nop 0
	v_cndmask_b32_e64 v4, v3, v4, s[18:19]
	v_fma_f32 v3, -v5, v3, v2
	v_cmp_lt_f32_e64 s[18:19], 0, v3
	s_nop 1
	v_cndmask_b32_e64 v3, v4, v5, s[18:19]
	v_mul_f32_e32 v4, 0x37800000, v3
	v_cndmask_b32_e32 v3, v3, v4, vcc
	v_mov_b32_e32 v4, 0x260
	v_cmp_class_f32_e32 vcc, v2, v4
	s_nop 1
	v_cndmask_b32_e32 v2, v3, v2, vcc
	s_nop 1
	v_add_f32_dpp v3, v2, v2 quad_perm:[1,0,3,2] row_mask:0xf bank_mask:0xf
	s_nop 1
	v_add_f32_dpp v4, v3, v3 quad_perm:[2,3,0,1] row_mask:0xf bank_mask:0xf
	s_nop 1
	v_add_f32_dpp v5, v4, v4 row_half_mirror row_mask:0xf bank_mask:0xf
	s_nop 1
	v_add_f32_dpp v6, v5, v5 row_mirror row_mask:0xf bank_mask:0xf
	s_nop 1
	v_readlane_b32 s12, v6, 0
	v_readlane_b32 s13, v6, 16
	v_readlane_b32 s14, v6, 32
	v_readlane_b32 s15, v6, 48
	s_nop 3
	v_mov_b32_e32 v7, s12
	v_add_f32_e32 v7, s13, v7
	v_mov_b32_e32 v9, s14
	v_add_f32_e32 v9, s15, v9
	v_add_f32_e32 v0, v7, v9
	v_mov_b32_e32 v4, 0
	s_mov_b64 exec, 1
	v_cvt_f64_f32_e32 v[6:7], v0
	v_add_f64 v[8:9], v[6:7], s[4:5]
	global_atomic_add_f64 v[10:11], v4, v[8:9], s[6:7] sc0
	s_waitcnt vmcnt(0)
	v_cmp_le_f64_e32 vcc, s[16:17], v[10:11]
	s_and_saveexec_b64 s[2:3], vcc
	s_cbranch_execz .Lmain_end
	v_add_f64 v[10:11], v[10:11], -s[16:17]
	v_add_f64 v[10:11], v[10:11], v[6:7]
	v_cvt_f32_f64_e32 v0, v[10:11]
	v_mul_f32_e32 v0, 0x38000000, v0
	global_atomic_add_f32 v4, v0, s[10:11]
